# speedup vs baseline: 1.0111x; 1.0055x over previous
.LBB3_33:
	s_waitcnt vmcnt(0) lgkmcnt(0)
	s_barrier
	s_add_i32 s60, s45, 16
	s_and_b32 s60, s60, 28
	s_or_b32 s60, s60, 2
	s_lshl_b32 s60, s60, 15
	s_lshr_b32 s62, s21, 1
	s_lshr_b32 s63, s20, 2
	s_xor_b32 s62, s62, s63
	s_and_b32 s62, s62, 1
	s_lshl_b32 s63, s62, 16
	v_add_u32_e32 v232, s63, v168
	v_add_u32_e32 v233, 0x8000, v232
	s_add_i32 s63, s45, 16
	s_and_b32 s63, s63, 28
	s_lshl_b32 s64, s62, 1
	s_or_b32 s63, s63, s64
	s_add_i32 s63, s63, s41
	s_lshl_b32 s63, s63, 1
	v_mov_b32_e32 v234, s63
	s_or_b32 s63, s63, 1
	v_mov_b32_e32 v235, s63
	s_lshl_b32 s64, s62, 8
	s_add_i32 s64, s64, s47
	s_add_i32 s64, s64, 0x20600
	v_lshl_add_u32 v236, v167, 2, s64
	s_movk_i32 s65, 0xffc0
	s_movk_i32 s66, 0xff80
	s_brev_b32 s67, -2
	s_add_i32 s68, s45, 12
	s_and_b32 s68, s68, 28
	s_or_b32 s68, s68, 2
	s_add_i32 s68, s68, s41
	s_lshl_b32 s68, s68, 1
	v_mov_b32_e32 v176, s68
	s_or_b32 s68, s68, 1
	v_mov_b32_e32 v177, s68
	s_add_i32 s68, s47, 0x20500
	v_lshl_add_u32 v182, v167, 2, s68
	ds_read_b128 v[144:147], v232 offset:0
	ds_read_b128 v[148:151], v232 offset:256
	ds_read_b128 v[152:155], v232 offset:2048
	ds_read_b128 v[156:159], v232 offset:2304
	ds_read_b128 v[224:227], v232 offset:4096
	s_waitcnt lgkmcnt(4)
	v_mfma_f32_16x16x32_bf16 v[208:211], v[0:3], v[144:147], 0
	v_mfma_f32_16x16x32_bf16 v[212:215], v[4:7], v[144:147], 0
	ds_read_b128 v[228:231], v232 offset:4352
	s_waitcnt lgkmcnt(4)
	v_mfma_f32_16x16x32_bf16 v[216:219], v[0:3], v[148:151], 0
	s_or_b32 s61, s60, 0x4000
	s_mov_b32 m0, s38
	s_nop 0
	buffer_load_dwordx4 v166, s[12:15], s61 offen lds
	v_mfma_f32_16x16x32_bf16 v[220:223], v[4:7], v[148:151], 0
	ds_read_b128 v[144:147], v232 offset:6144
	s_waitcnt lgkmcnt(4)
	v_mfma_f32_16x16x32_bf16 v[208:211], v[8:11], v[152:155], v[208:211]
	v_mfma_f32_16x16x32_bf16 v[212:215], v[12:15], v[152:155], v[212:215]
	ds_read_b128 v[148:151], v232 offset:6400
	v_and_or_b32 v180, v136, s65, v176
	v_and_or_b32 v181, v140, s65, v177
	v_max3_f32 v161, v161, v180, v181
	v_and_b32_e32 v178, 0xffffff80, v136
	v_and_b32_e32 v179, 0xffffff80, v140
	s_waitcnt lgkmcnt(4)
	v_mfma_f32_16x16x32_bf16 v[216:219], v[8:11], v[156:159], v[216:219]
	s_or_b32 s61, s60, 0x6000
	s_mov_b32 m0, s39
	s_nop 0
	buffer_load_dwordx4 v166, s[12:15], s61 offen lds
	v_mfma_f32_16x16x32_bf16 v[220:223], v[12:15], v[156:159], v[220:223]
	ds_read_b128 v[152:155], v232 offset:8192
	v_and_or_b32 v180, v137, s65, v176
	v_and_or_b32 v181, v141, s65, v177
	v_max3_f32 v160, v160, v180, v181
	v_and_or_b32 v180, v137, s66, 1
	v_and_or_b32 v181, v141, s66, 1
	v_max_f32_e32 v178, v178, v180
	v_max_f32_e32 v179, v179, v181
	s_waitcnt lgkmcnt(4)
	v_mfma_f32_16x16x32_bf16 v[208:211], v[16:19], v[224:227], v[208:211]
	v_mfma_f32_16x16x32_bf16 v[212:215], v[20:23], v[224:227], v[212:215]
	ds_read_b128 v[156:159], v232 offset:8448
	v_and_or_b32 v180, v138, s65, v176
	v_and_or_b32 v181, v142, s65, v177
	v_max3_f32 v162, v162, v180, v181
	v_and_or_b32 v180, v138, s66, 2
	v_and_or_b32 v181, v142, s66, 2
	v_max_f32_e32 v178, v178, v180
	v_max_f32_e32 v179, v179, v181
	s_waitcnt lgkmcnt(4)
	v_mfma_f32_16x16x32_bf16 v[216:219], v[16:19], v[228:231], v[216:219]
	s_or_b32 s61, s60, 0xc000
	s_mov_b32 m0, s40
	s_nop 0
	buffer_load_dwordx4 v166, s[12:15], s61 offen lds
	v_mfma_f32_16x16x32_bf16 v[220:223], v[20:23], v[228:231], v[220:223]
	ds_read_b128 v[224:227], v232 offset:10240
	v_and_or_b32 v180, v139, s65, v176
	v_and_or_b32 v181, v143, s65, v177
	v_max3_f32 v163, v163, v180, v181
	v_and_or_b32 v180, v139, s66, 3
	v_and_or_b32 v181, v143, s66, 3
	v_max_f32_e32 v178, v178, v180
	v_max_f32_e32 v179, v179, v181
	s_waitcnt lgkmcnt(4)
	v_mfma_f32_16x16x32_bf16 v[208:211], v[24:27], v[144:147], v[208:211]
	v_mfma_f32_16x16x32_bf16 v[212:215], v[28:31], v[144:147], v[212:215]
	ds_read_b128 v[228:231], v232 offset:10496
	v_and_or_b32 v180, v128, s65, v176
	v_and_or_b32 v181, v132, s65, v177
	v_max3_f32 v203, v203, v180, v181
	v_and_or_b32 v180, v128, s66, 4
	v_and_or_b32 v181, v132, s66, 4
	v_max_f32_e32 v178, v178, v180
	v_max_f32_e32 v179, v179, v181
	s_waitcnt lgkmcnt(4)
	v_mfma_f32_16x16x32_bf16 v[216:219], v[24:27], v[148:151], v[216:219]
	s_or_b32 s61, s60, 0xe000
	s_mov_b32 m0, s42
	s_nop 0
	buffer_load_dwordx4 v166, s[12:15], s61 offen lds
	v_mfma_f32_16x16x32_bf16 v[220:223], v[28:31], v[148:151], v[220:223]
	ds_read_b128 v[144:147], v232 offset:12288
	v_and_or_b32 v180, v129, s65, v176
	v_and_or_b32 v181, v133, s65, v177
	v_max3_f32 v204, v204, v180, v181
	v_and_or_b32 v180, v129, s66, 5
	v_and_or_b32 v181, v133, s66, 5
	v_max_f32_e32 v178, v178, v180
	v_max_f32_e32 v179, v179, v181
	s_waitcnt lgkmcnt(4)
	v_mfma_f32_16x16x32_bf16 v[208:211], v[32:35], v[152:155], v[208:211]
	v_mfma_f32_16x16x32_bf16 v[212:215], v[36:39], v[152:155], v[212:215]
	ds_read_b128 v[148:151], v232 offset:12544
	v_and_or_b32 v180, v130, s65, v176
	v_and_or_b32 v181, v134, s65, v177
	v_max3_f32 v205, v205, v180, v181
	v_and_or_b32 v180, v130, s66, 6
	v_and_or_b32 v181, v134, s66, 6
	v_max_f32_e32 v178, v178, v180
	v_max_f32_e32 v179, v179, v181
	s_waitcnt lgkmcnt(4)
	v_mfma_f32_16x16x32_bf16 v[216:219], v[32:35], v[156:159], v[216:219]
	v_mfma_f32_16x16x32_bf16 v[220:223], v[36:39], v[156:159], v[220:223]
	ds_read_b128 v[152:155], v232 offset:14336
	v_and_or_b32 v180, v131, s65, v176
	v_and_or_b32 v181, v135, s65, v177
	v_max3_f32 v206, v206, v180, v181
	v_and_or_b32 v180, v131, s66, 7
	v_and_or_b32 v181, v135, s66, 7
	v_max_f32_e32 v178, v178, v180
	v_max_f32_e32 v179, v179, v181
	s_waitcnt lgkmcnt(4)
	v_mfma_f32_16x16x32_bf16 v[208:211], v[40:43], v[224:227], v[208:211]
	v_mfma_f32_16x16x32_bf16 v[212:215], v[44:47], v[224:227], v[212:215]
	ds_read_b128 v[156:159], v232 offset:14592
	v_or_b32_e32 v183, v173, v178
	v_ashrrev_i32_e32 v180, 31, v178
	v_bitop3_b32 v183, v180, v183, s67 bitop3:0x6c
	v_or_b32_e32 v184, v173, v179
	v_ashrrev_i32_e32 v181, 31, v179
	v_bitop3_b32 v184, v181, v184, s67 bitop3:0x6c
	s_waitcnt lgkmcnt(4)
	v_mfma_f32_16x16x32_bf16 v[216:219], v[40:43], v[228:231], v[216:219]
	v_mfma_f32_16x16x32_bf16 v[220:223], v[44:47], v[228:231], v[220:223]
	s_waitcnt lgkmcnt(3)
	v_mfma_f32_16x16x32_bf16 v[208:211], v[48:51], v[144:147], v[208:211]
	v_mfma_f32_16x16x32_bf16 v[212:215], v[52:55], v[144:147], v[212:215]
	s_waitcnt lgkmcnt(2)
	v_mfma_f32_16x16x32_bf16 v[216:219], v[48:51], v[148:151], v[216:219]
	v_mfma_f32_16x16x32_bf16 v[220:223], v[52:55], v[148:151], v[220:223]
	s_waitcnt lgkmcnt(1)
	v_mfma_f32_16x16x32_bf16 v[208:211], v[56:59], v[152:155], v[208:211]
	v_mfma_f32_16x16x32_bf16 v[212:215], v[60:63], v[152:155], v[212:215]
	s_waitcnt lgkmcnt(0)
	v_mfma_f32_16x16x32_bf16 v[216:219], v[56:59], v[156:159], v[216:219]
	v_mfma_f32_16x16x32_bf16 v[220:223], v[60:63], v[156:159], v[220:223]
	s_waitcnt vmcnt(0)
	s_barrier
	ds_read_b128 v[144:147], v233 offset:0
	ds_read_b128 v[148:151], v233 offset:256
	ds_read_b128 v[152:155], v233 offset:2048
	ds_read_b128 v[156:159], v233 offset:2304
	ds_read_b128 v[224:227], v233 offset:4096
	s_waitcnt lgkmcnt(4)
	v_mfma_f32_16x16x32_bf16 v[208:211], v[64:67], v[144:147], v[208:211]
	v_mfma_f32_16x16x32_bf16 v[212:215], v[68:71], v[144:147], v[212:215]
	ds_read_b128 v[228:231], v233 offset:4352
	s_waitcnt lgkmcnt(4)
	v_mfma_f32_16x16x32_bf16 v[216:219], v[64:67], v[148:151], v[216:219]
	v_mfma_f32_16x16x32_bf16 v[220:223], v[68:71], v[148:151], v[220:223]
	ds_read_b128 v[144:147], v233 offset:6144
	s_waitcnt lgkmcnt(4)
	v_mfma_f32_16x16x32_bf16 v[208:211], v[72:75], v[152:155], v[208:211]
	v_mfma_f32_16x16x32_bf16 v[212:215], v[76:79], v[152:155], v[212:215]
	ds_read_b128 v[148:151], v233 offset:6400
	s_waitcnt lgkmcnt(4)
	v_mfma_f32_16x16x32_bf16 v[216:219], v[72:75], v[156:159], v[216:219]
	v_mfma_f32_16x16x32_bf16 v[220:223], v[76:79], v[156:159], v[220:223]
	ds_read_b128 v[152:155], v233 offset:8192
	s_waitcnt lgkmcnt(4)
	v_mfma_f32_16x16x32_bf16 v[208:211], v[80:83], v[224:227], v[208:211]
	v_mfma_f32_16x16x32_bf16 v[212:215], v[84:87], v[224:227], v[212:215]
	ds_read_b128 v[156:159], v233 offset:8448
	s_waitcnt lgkmcnt(4)
	v_mfma_f32_16x16x32_bf16 v[216:219], v[80:83], v[228:231], v[216:219]
	v_mfma_f32_16x16x32_bf16 v[220:223], v[84:87], v[228:231], v[220:223]
	ds_read_b128 v[224:227], v233 offset:10240
	s_waitcnt lgkmcnt(4)
	v_mfma_f32_16x16x32_bf16 v[208:211], v[88:91], v[144:147], v[208:211]
	v_mfma_f32_16x16x32_bf16 v[212:215], v[92:95], v[144:147], v[212:215]
	ds_read_b128 v[228:231], v233 offset:10496
	s_waitcnt lgkmcnt(4)
	v_mfma_f32_16x16x32_bf16 v[216:219], v[88:91], v[148:151], v[216:219]
	v_mfma_f32_16x16x32_bf16 v[220:223], v[92:95], v[148:151], v[220:223]
	ds_read_b128 v[144:147], v233 offset:12288
	s_waitcnt lgkmcnt(4)
	v_mfma_f32_16x16x32_bf16 v[208:211], v[96:99], v[152:155], v[208:211]
	v_mfma_f32_16x16x32_bf16 v[212:215], v[100:103], v[152:155], v[212:215]
	ds_read_b128 v[148:151], v233 offset:12544
	s_waitcnt lgkmcnt(4)
	v_mfma_f32_16x16x32_bf16 v[216:219], v[96:99], v[156:159], v[216:219]
	v_mfma_f32_16x16x32_bf16 v[220:223], v[100:103], v[156:159], v[220:223]
	ds_read_b128 v[152:155], v233 offset:14336
	s_waitcnt lgkmcnt(4)
	v_mfma_f32_16x16x32_bf16 v[208:211], v[104:107], v[224:227], v[208:211]
	v_mfma_f32_16x16x32_bf16 v[212:215], v[108:111], v[224:227], v[212:215]
	ds_read_b128 v[156:159], v233 offset:14592
	s_waitcnt lgkmcnt(4)
	v_mfma_f32_16x16x32_bf16 v[216:219], v[104:107], v[228:231], v[216:219]
	v_mfma_f32_16x16x32_bf16 v[220:223], v[108:111], v[228:231], v[220:223]
	s_waitcnt lgkmcnt(3)
	v_mfma_f32_16x16x32_bf16 v[208:211], v[112:115], v[144:147], v[208:211]
	v_mfma_f32_16x16x32_bf16 v[212:215], v[116:119], v[144:147], v[212:215]
	s_waitcnt lgkmcnt(2)
	v_mfma_f32_16x16x32_bf16 v[216:219], v[112:115], v[148:151], v[216:219]
	v_mfma_f32_16x16x32_bf16 v[220:223], v[116:119], v[148:151], v[220:223]
	s_waitcnt lgkmcnt(1)
	v_mfma_f32_16x16x32_bf16 v[208:211], v[120:123], v[152:155], v[208:211]
	v_mfma_f32_16x16x32_bf16 v[212:215], v[124:127], v[152:155], v[212:215]
	s_waitcnt lgkmcnt(0)
	v_mfma_f32_16x16x32_bf16 v[216:219], v[120:123], v[156:159], v[216:219]
	v_mfma_f32_16x16x32_bf16 v[220:223], v[124:127], v[156:159], v[220:223]
	s_nop 7
	s_nop 3
	v_and_or_b32 v237, v208, s65, v234
	v_and_or_b32 v238, v216, s65, v235
	v_max3_f32 v161, v161, v237, v238
	v_and_b32_e32 v174, 0xffffff80, v208
	v_and_b32_e32 v175, 0xffffff80, v216
	v_and_or_b32 v237, v209, s65, v234
	v_and_or_b32 v238, v217, s65, v235
	v_max3_f32 v160, v160, v237, v238
	v_and_or_b32 v237, v209, s66, 1
	v_and_or_b32 v238, v217, s66, 1
	v_max_f32_e32 v174, v174, v237
	v_max_f32_e32 v175, v175, v238
	v_and_or_b32 v237, v210, s65, v234
	v_and_or_b32 v238, v218, s65, v235
	v_max3_f32 v162, v162, v237, v238
	v_and_or_b32 v237, v210, s66, 2
	v_and_or_b32 v238, v218, s66, 2
	v_max_f32_e32 v174, v174, v237
	v_max_f32_e32 v175, v175, v238
	v_and_or_b32 v237, v211, s65, v234
	v_and_or_b32 v238, v219, s65, v235
	v_max3_f32 v163, v163, v237, v238
	v_and_or_b32 v237, v211, s66, 3
	v_and_or_b32 v238, v219, s66, 3
	v_max_f32_e32 v174, v174, v237
	v_max_f32_e32 v175, v175, v238
	v_and_or_b32 v237, v212, s65, v234
	v_and_or_b32 v238, v220, s65, v235
	v_max3_f32 v203, v203, v237, v238
	v_and_or_b32 v237, v212, s66, 4
	v_and_or_b32 v238, v220, s66, 4
	v_max_f32_e32 v174, v174, v237
	v_max_f32_e32 v175, v175, v238
	v_and_or_b32 v237, v213, s65, v234
	v_and_or_b32 v238, v221, s65, v235
	v_max3_f32 v204, v204, v237, v238
	v_and_or_b32 v237, v213, s66, 5
	v_and_or_b32 v238, v221, s66, 5
	v_max_f32_e32 v174, v174, v237
	v_max_f32_e32 v175, v175, v238
	v_and_or_b32 v237, v214, s65, v234
	v_and_or_b32 v238, v222, s65, v235
	v_max3_f32 v205, v205, v237, v238
	v_and_or_b32 v237, v214, s66, 6
	v_and_or_b32 v238, v222, s66, 6
	v_max_f32_e32 v174, v174, v237
	v_max_f32_e32 v175, v175, v238
	v_and_or_b32 v237, v215, s65, v234
	v_and_or_b32 v238, v223, s65, v235
	v_max3_f32 v206, v206, v237, v238
	v_and_or_b32 v237, v215, s66, 7
	v_and_or_b32 v238, v223, s66, 7
	v_max_f32_e32 v174, v174, v237
	v_max_f32_e32 v175, v175, v238
	v_or_b32_e32 v237, v173, v174
	v_ashrrev_i32_e32 v238, 31, v174
	v_bitop3_b32 v237, v238, v237, s67 bitop3:0x6c
	ds_max_i32 v236, v237
	v_or_b32_e32 v237, v173, v175
	v_ashrrev_i32_e32 v238, 31, v175
	v_bitop3_b32 v237, v238, v237, s67 bitop3:0x6c
	ds_max_i32 v236, v237 offset:64
	ds_max_i32 v182, v183
	ds_max_i32 v182, v184 offset:64
	v_mov_b32_e32 v0, v161
	v_mov_b32_e32 v1, v160
	v_mov_b32_e32 v3, v162
	v_mov_b32_e32 v4, v163
	v_mov_b32_e32 v5, v203
	v_mov_b32_e32 v6, v204
	v_mov_b32_e32 v7, v205
	v_mov_b32_e32 v8, v206
	s_movk_i32 s2, 0xff80
	s_brev_b32 s3, -2
	v_mbcnt_lo_u32_b32 v2, -1, 0
	s_andn2_b32 s23, s23, 63
	s_lshl_b64 s[0:1], s[16:17], 13
	s_waitcnt vmcnt(0)
	v_mbcnt_hi_u32_b32 v2, -1, v2
	s_add_u32 s4, s10, s0
	v_add_u32_e32 v9, s23, v2
	s_addc_u32 s5, s11, s1
	s_mov_b32 s6, 4
	s_lshl_b32 s0, s6, 7
	v_cmp_gt_i32_e32 vcc, s0, v9
	s_waitcnt lgkmcnt(0)
	s_barrier
	s_and_saveexec_b64 s[0:1], vcc
	s_cbranch_execz .LBB3_35
	v_mov_b32_e32 v10, 0x20000
	v_lshl_add_u32 v10, v9, 2, v10
	ds_read_b32 v10, v10
	s_movk_i32 s6, 0x63
	v_and_b32_e32 v12, 0x7f, v9
	s_waitcnt lgkmcnt(0)
	v_ashrrev_i32_e32 v11, 31, v10
	v_and_b32_e32 v13, 0x7fffffff, v11
	v_bitop3_b32 v11, v11, v10, s3 bitop3:0x6c
	v_lshlrev_b32_e32 v14, 2, v11
	v_and_b32_e32 v14, 16, v14
	s_lshl_b32 s3, s20, 7
	v_bitop3_b32 v13, v13, s6, v10 bitop3:0x48
	v_or3_b32 v13, v13, s3, v14
	v_bfrev_b32_e32 v14, 1
	v_cmp_lt_i32_e32 vcc, -1, v10
	v_lshrrev_b32_e32 v15, 1, v11
	v_and_b32_e32 v15, 12, v15
	v_cndmask_b32_e32 v10, -1, v14, vcc
	v_bitop3_b32 v11, v11, v10, s2 bitop3:0x6c
	s_movk_i32 s2, 0x3ff
	v_bitop3_b32 v10, v13, s2, v15 bitop3:0x36
	s_lshl_b32 s2, s22, 7
	s_addk_i32 s2, 0x80
	v_add_u32_e32 v9, s2, v9
	s_movk_i32 s2, 0x380
	v_and_or_b32 v9, v9, s2, v12
	v_lshlrev_b32_e32 v9, 3, v9
	global_atomic_umax_x2 v9, v[10:11], s[4:5]
